# own-layer conversion with the 2-of-5 ticket pattern in every layer (layer 0: 1536 items)
# speedup vs baseline: 1.0181x; 1.0084x over previous
.LBB0_789:
	s_or_b64 exec, exec, s[2:3]
	v_readlane_b32 s2, v253, 55
	s_waitcnt lgkmcnt(0)
	s_barrier
	v_mov_b32_e32 v0, s2
	v_readlane_b32 s2, v253, 54
	ds_read_b32 v0, v0
	s_nop 0
	v_mov_b32_e32 v1, s2
	ds_read_b32 v1, v1
	s_waitcnt lgkmcnt(0)
	s_barrier
	v_add_u32_e32 v201, 0x580, v0
	s_nop 0
	v_readfirstlane_b32 s100, v201
	v_readlane_b32 s101, v254, 38
	s_nop 3
	s_movk_i32 vcc_lo, 0x4c0
	s_movk_i32 vcc_hi, 0xbe0
	s_cmp_eq_u32 s101, 0
	s_cselect_b32 vcc_lo, 0x600, vcc_lo
	s_cselect_b32 vcc_hi, 0xf00, vcc_hi
	s_add_i32 vcc_lo, s100, vcc_lo
	s_max_u32 vcc_lo, vcc_lo, vcc_hi
	v_mov_b32_e32 v201, vcc_lo
	v_readfirstlane_b32 s30, v0
	v_cmp_ge_i32_e32 vcc, v1, v201
	v_readfirstlane_b32 s24, v1
	s_cbranch_vccnz .LBB0_931
	s_add_u32 s31, s4, 0x37b00000
	s_addc_u32 s34, s5, 0
	s_add_i32 s35, s30, 0x480
	s_add_u32 s44, s4, 0x61800000
	s_addc_u32 s45, s5, 0
	s_add_u32 s46, s4, 0x42c00000
	s_addc_u32 s47, s5, 0
	s_add_u32 s10, s4, 0x66d00000
	s_addc_u32 s11, s5, 0
	s_add_u32 s48, s4, 0x61640000
	s_movk_i32 s2, 0x100
	s_addc_u32 s49, s5, 0
	v_cmp_gt_i32_e64 s[38:39], s2, v199
	s_add_i32 s2, 0, 0x14800
	v_add_u32_e32 v214, s2, v200
	s_add_i32 s2, 0, 0x16800
	s_cmp_lg_u32 0, -1
	v_lshlrev_b32_e32 v3, 1, v199
	v_lshlrev_b32_e32 v211, 4, v199
	s_cselect_b32 s3, 0, 0
	v_lshlrev_b32_e32 v0, 3, v199
	v_lshlrev_b32_e32 v1, 10, v101
	v_lshlrev_b32_e32 v2, 4, v198
	v_and_b32_e32 v3, 32, v3
	v_and_b32_e32 v5, 0xc0, v211
	s_addk_i32 s3, 0x6000
	v_and_b32_e32 v210, 24, v0
	v_lshl_or_b32 v5, v101, 8, v5
	v_add3_u32 v213, 0, v1, v2
	v_add_u32_e32 v1, s3, v3
	v_add3_u32 v217, v1, v210, v5
	v_lshrrev_b32_e32 v1, 3, v100
	v_lshl_add_u32 v215, v198, 2, s2
	v_and_b32_e32 v218, 56, v0
	v_lshl_add_u32 v220, v1, 2, s2
	s_add_i32 s2, 0, 0x14a00
	v_add_u32_e32 v4, 0, v3
	v_lshlrev_b32_e32 v96, 1, v218
	v_add_u32_e32 v221, s2, v200
	s_add_i32 s2, 0, 0x14900
	v_ashrrev_i32_e32 v203, 31, v202
	v_lshlrev_b32_e32 v208, 9, v100
	v_lshrrev_b32_e32 v209, 2, v100
	v_add3_u32 v212, v4, v210, v5
	v_cmp_gt_u32_e64 s[40:41], 32, v100
	v_cmp_lt_u32_e64 s[42:43], 31, v100
	v_or_b32_e32 v216, 0xc0, v206
	v_lshl_add_u64 v[204:205], s[4:5], 0, v[96:97]
	v_lshlrev_b32_e32 v219, 7, v1
	v_add_u32_e32 v222, s2, v200
	v_lshlrev_b32_e32 v96, 1, v98
	s_branch .LBB0_792

.Lc3_pat:
	s_mul_hi_u32 s101, s24, 0xcccccccd
	s_lshr_b32 s101, s101, 2
	s_mul_i32 s2, s101, 5
	s_sub_i32 s2, s24, s2
	s_lshl_b32 s101, s101, 1
	s_cmp_eq_u32 s2, 1
	s_cbranch_scc1 .Lc3_entry
	s_cmp_eq_u32 s2, 3
	s_cbranch_scc0 .Lc3_r5a
	s_add_i32 s101, s101, 1
	s_branch .Lc3_entry

.Lc3_l0:
	s_cmpk_lt_u32 s24, 0xf00
	s_cbranch_scc1 .Lc3_pat
